# baseline (speedup 1.0000x reference)
.LBB0_118:
	s_or_b64 exec, exec, s[60:61]
	v_readfirstlane_b32 s74, v0
	v_mov_b32_e32 v42, 0
	v_mov_b32_e32 v50, 0
	v_bfe_u32 v36, v0, 8, 2
	v_lshl_or_b32 v44, v36, 13, v86
	v_mov_b32_e32 v45, 0
	v_lshl_add_u64 v[18:19], s[56:57], 0, v[44:45]
	v_add_co_u32_e32 v34, vcc, 0x1000, v18
	global_load_dwordx4 v[2:5], v44, s[56:57]
	global_load_dwordx4 v[6:9], v44, s[56:57] offset:1024
	global_load_dwordx4 v[10:13], v44, s[56:57] offset:2048
	global_load_dwordx4 v[14:17], v44, s[56:57] offset:3072
	v_addc_co_u32_e32 v35, vcc, 0, v19, vcc
	v_lshlrev_b32_e32 v44, 7, v36
	global_load_dwordx4 v[18:21], v[34:35], off
	global_load_dwordx4 v[22:25], v[34:35], off offset:1024
	global_load_dwordx4 v[26:29], v[34:35], off offset:2048
	global_load_dwordx4 v[30:33], v[34:35], off offset:3072
	v_lshl_add_u64 v[34:35], s[52:53], 0, v[44:45]
	v_lshlrev_b32_e32 v36, 2, v1
	v_mov_b32_e32 v37, v45
	v_lshl_add_u64 v[46:47], v[34:35], 0, v[36:37]
	global_load_dwordx4 v[34:37], v[46:47], off offset:16
	global_load_dwordx4 v[38:41], v[46:47], off
	v_add3_u32 v46, s66, v50, v79
	v_ashrrev_i32_e32 v47, 31, v46
	v_and_b32_e32 v0, 48, v0
	v_lshlrev_b64 v[46:47], 9, v[46:47]
	v_lshlrev_b32_e32 v0, 1, v0
	v_or3_b32 v46, v46, v44, v0
	v_mul_u32_u24_e32 v43, 0x110, v79
	s_movk_i32 s0, 0x1100
	v_lshl_add_u64 v[0:1], s[54:55], 0, v[46:47]
	v_mad_u32_u24 v42, v42, s0, v43
	s_mov_b32 s0, 0x10000
	v_lshl_add_u64 v[0:1], v[0:1], 0, 16
	v_add3_u32 v51, v42, v70, s0
	s_lshr_b32 s74, s74, 8
	s_and_b32 s74, s74, 3
	s_lshl_b32 s75, s74, 2
	s_add_i32 s75, s75, 0x26d50
	s_add_i32 s76, s33, 15
	s_lshr_b32 s76, s76, 4
	v_mov_b64_e32 v[60:61], v[0:1]
	v_mov_b32_e32 v62, v51
	s_waitcnt vmcnt(0)
